# P3 conversion fill spread: one tile on each of workgroups 64..255 instead of three on 192..255
# baseline (speedup 1.0000x reference)
; __device__ __forceinline__ void conv8_fill(const Ctx& X, int base, int rank, int nblk, int n) { conv8b_run(X, (base >> 3) + rank, nblk, n); }
; #define SEAM(k) do { if (IN(k) && IN((k) + 1)) xcd_barrier(bar); } while (0)
; __device__ __forceinline__ Cvb conv8b_dec(const Ctx& X, int bit) { Cvb c; int kb, nb;
;     if (bit < I_GU8 / 8) { const int e = bit >> 8, r = bit & 255; kb = r >> 4; nb = r & 15; c.N = 2 * DFF; c.W = XP_w_gu(X) + (size_t)e * D * (2 * DFF); c.WT = XP_WguT(X) + (size_t)e * 16 * PAN_GU + (size_t)kb * PAN_GU; }
;     else { const int b2 = bit - I_GU8 / 8, e = b2 >> 7, r = b2 & 127; kb = r >> 3; nb = r & 7; c.N = D; c.W = XP_w_d(X) + (size_t)e * DFF * D; c.WT = XP_WdT(X) + (size_t)e * 16 * PAN_D + (size_t)kb * PAN_D; }
;     c.W += (size_t)(kb * 128 + 16 * X.wave) * c.N + nb * 256 + 4 * X.lane;
;     c.WT += (size_t)(nb * 256 + 32 * X.wave + (X.lane >> 3)) * 128 + 16 * (X.lane & 7);
;     return c; }
; __device__ __forceinline__ void conv8b_run(const Ctx& X, int first, int step, int count) {
;     if (count <= 0) return;
;     f32x4 v[16];
;     Cvb c = conv8b_dec(X, first), cn = c;
; #pragma unroll
;     for (int i = 0; i < 16; ++i) v[i] = __builtin_nontemporal_load((const f32x4*)(c.W + (size_t)i * c.N));
; __global__ void __launch_bounds__(NTHR, 2) fwd(Args args) {
;     ...
;     if (IN(3)) { p3_scan(X); if (X.G == 256 && X.bid >= 192) conv8_fill(X, FILL_B3, X.bid - 192, FILL_W3 / NWAVES, FILL_N3); } SEAM(3);
.LBB0_474:
	s_or_b64 exec, exec, s[6:7]
	s_cmpk_lg_i32 s92, 0x100
	s_cselect_b64 s[2:3], -1, 0
	s_cmpk_lt_i32 s87, 0x40
	s_cselect_b64 s[6:7], -1, 0
	s_or_b64 s[2:3], s[6:7], s[2:3]
	s_and_b64 vcc, exec, s[2:3]
	s_cbranch_vccnz .LBB0_480
	s_load_dwordx2 s[6:7], s[0:1], 0x80
	s_add_i32 s2, s87, 0x980
	s_lshr_b32 s2, s2, 7
	s_mov_b32 s3, 0
	s_bfe_u32 s13, s87, 0x40003
	s_lshl_b64 s[8:9], s[2:3], 24
	s_waitcnt lgkmcnt(0)
	s_add_u32 s14, s6, s8
	s_addc_u32 s15, s7, s9
	s_add_u32 s10, s90, 0x50000000
	s_addc_u32 s11, s91, 0
	s_lshl_b64 s[6:7], s[2:3], 22
	s_add_u32 s2, s10, s6
	s_addc_u32 s7, s11, s7
	s_lshl_b32 s6, s13, 18
	s_add_u32 s6, s2, s6
	s_addc_u32 s7, s7, 0
	s_lshl_b32 s2, s87, 8
	s_lshl_b32 s16, s93, 5
	s_and_b32 s17, s2, 0x700
	s_add_i32 s2, s16, s17
	v_lshrrev_b32_e32 v75, 3, v194
	v_or_b32_e32 v66, s2, v75
	s_lshl_b32 s12, s93, 4
	s_lshl_b32 s2, s13, 7
	s_add_i32 s2, s12, s2
	s_lshl_b64 s[8:9], s[2:3], 13
	s_add_u32 s2, s14, s8
	s_addc_u32 s9, s15, s9
	s_lshl_b32 s8, s17, 2
	v_mov_b32_e32 v67, 0
	s_add_u32 s8, s2, s8
	v_lshlrev_b64 v[68:69], 7, v[66:67]
	s_addc_u32 s9, s9, 0
	v_lshlrev_b32_e32 v66, 4, v194
	s_waitcnt vmcnt(3)
	v_lshl_add_u64 v[30:31], s[8:9], 0, v[66:67]
	s_mov_b32 s2, 0x1e000
	v_add_co_u32_e32 v6, vcc, s2, v30
	s_mov_b32 s2, 0x1c000
	s_nop 0
	v_addc_co_u32_e32 v7, vcc, 0, v31, vcc
	v_add_co_u32_e32 v8, vcc, s2, v30
	s_mov_b32 s2, 0x1a000
	s_nop 0
	v_addc_co_u32_e32 v9, vcc, 0, v31, vcc
	v_add_co_u32_e32 v10, vcc, s2, v30
	s_mov_b32 s2, 0x18000
	s_nop 0
	v_addc_co_u32_e32 v11, vcc, 0, v31, vcc
	v_add_co_u32_e32 v12, vcc, s2, v30
	s_mov_b32 s2, 0x16000
	s_nop 0
	v_addc_co_u32_e32 v13, vcc, 0, v31, vcc
	v_add_co_u32_e32 v14, vcc, s2, v30
	s_mov_b32 s2, 0x14000
	s_nop 0
	v_addc_co_u32_e32 v15, vcc, 0, v31, vcc
	v_add_co_u32_e32 v16, vcc, s2, v30
	s_mov_b32 s2, 0x12000
	s_nop 0
	v_addc_co_u32_e32 v17, vcc, 0, v31, vcc
	v_add_co_u32_e32 v18, vcc, s2, v30
	s_mov_b32 s2, 0x10000
	s_nop 0
	v_addc_co_u32_e32 v19, vcc, 0, v31, vcc
	v_add_co_u32_e32 v20, vcc, s2, v30
	s_mov_b32 s2, 0xe000
	s_nop 0
	v_addc_co_u32_e32 v21, vcc, 0, v31, vcc
	v_add_co_u32_e32 v22, vcc, s2, v30
	s_mov_b32 s2, 0xc000
	s_nop 0
	v_addc_co_u32_e32 v23, vcc, 0, v31, vcc
	v_add_co_u32_e32 v24, vcc, s2, v30
	s_mov_b32 s2, 0xa000
	s_nop 0
	v_addc_co_u32_e32 v25, vcc, 0, v31, vcc
	v_add_co_u32_e32 v26, vcc, s2, v30
	s_mov_b32 s2, 0x8000
	s_nop 0
	v_addc_co_u32_e32 v27, vcc, 0, v31, vcc
	v_add_co_u32_e32 v28, vcc, s2, v30
	s_movk_i32 s2, 0x6000
	s_nop 0
	v_addc_co_u32_e32 v29, vcc, 0, v31, vcc
	v_add_co_u32_e32 v32, vcc, s2, v30
	s_movk_i32 s2, 0x4000
	s_nop 0
	v_addc_co_u32_e32 v33, vcc, 0, v31, vcc
	s_waitcnt vmcnt(0)
	v_add_co_u32_e32 v62, vcc, s2, v30
	s_movk_i32 s2, 0x2000
	s_nop 0
	v_addc_co_u32_e32 v63, vcc, 0, v31, vcc
	v_add_co_u32_e32 v70, vcc, s2, v30
	global_load_dwordx4 v[34:37], v[6:7], off nt
	global_load_dwordx4 v[2:5], v[8:9], off nt
	v_addc_co_u32_e32 v71, vcc, 0, v31, vcc
	global_load_dwordx4 v[38:41], v[10:11], off nt
	global_load_dwordx4 v[6:9], v[12:13], off nt
	global_load_dwordx4 v[42:45], v[14:15], off nt
	s_nop 0
	global_load_dwordx4 v[10:13], v[16:17], off nt
	global_load_dwordx4 v[46:49], v[18:19], off nt
	s_nop 0
	global_load_dwordx4 v[14:17], v[20:21], off nt
	global_load_dwordx4 v[50:53], v[22:23], off nt
	s_nop 0
	global_load_dwordx4 v[18:21], v[24:25], off nt
	global_load_dwordx4 v[54:57], v[26:27], off nt
	s_nop 0
	global_load_dwordx4 v[22:25], v[28:29], off nt
	global_load_dwordx4 v[58:61], v[32:33], off nt
	s_nop 0
	global_load_dwordx4 v[26:29], v[62:63], off nt
	global_load_dwordx4 v[30:33], v[70:71], off nt
	s_nop 0
	global_load_dwordx4 v[62:65], v66, s[8:9] nt
	v_lshlrev_b32_e32 v66, 4, v0
	v_lshl_add_u64 v[70:71], s[6:7], 0, v[68:69]
	v_and_b32_e32 v68, 0x70, v66
	v_mov_b32_e32 v69, v67
	v_or_b32_e32 v66, s16, v75
	s_movk_i32 s2, 0x90
	v_lshl_add_u64 v[72:73], v[70:71], 0, v[68:69]
	v_lshlrev_b32_e32 v74, 2, v194
	v_mul_lo_u32 v77, v66, s2
	v_add_u32_e32 v66, s17, v66
	v_mul_u32_u24_e32 v76, 0x240, v194
	v_lshlrev_b64 v[70:71], 7, v[66:67]
	s_add_i32 s13, s87, 0x2940
	s_mov_b32 s14, 0xc3e00000
	s_lshl_b32 s15, s17, 2
	v_lshlrev_b32_e32 v66, 2, v74
	v_mov_b32_e32 v78, 0x43e00000
	s_mov_b32 s16, 0
	v_mov_b64_e32 v[74:75], v[72:73]
	s_branch .LBB0_477
.LBB0_476:
	v_add3_u32 v79, s17, v77, v68
	s_waitcnt lgkmcnt(0)
	s_barrier
	ds_read_b128 v[80:83], v79
	ds_read_b128 v[84:87], v79 offset:1152
	ds_read_b128 v[88:91], v79 offset:2304
	ds_read_b128 v[92:95], v79 offset:3456
	s_add_i32 s16, s16, 1
	s_add_i32 s13, s13, 64
	s_waitcnt lgkmcnt(3)
	global_store_dwordx4 v[72:73], v[80:83], off nt
	s_waitcnt lgkmcnt(2)
	global_store_dwordx4 v[72:73], v[84:87], off offset:1024 nt
	s_waitcnt lgkmcnt(1)
	global_store_dwordx4 v[72:73], v[88:91], off offset:2048 nt
	s_waitcnt lgkmcnt(0)
	global_store_dwordx4 v[72:73], v[92:95], off offset:3072 nt
	s_cmp_lg_u32 s16, 1
	v_mov_b64_e32 v[72:73], v[74:75]
	s_cbranch_scc0 .LBB0_479
; #define LAS __attribute__((address_space(3)))
; __device__ __forceinline__ void conv8b_run(const Ctx& X, int first, int step, int count) {
;     ...
;         LAS uchar* buf = X.lds + (j & 1) * CVT_BUF;
; #pragma unroll
;         for (int q = 0; q < 4; ++q) { u32x4 o;
;             o.x = pk_fp8x4(v[0][q] * W8_SCALE, v[1][q] * W8_SCALE, v[2][q] * W8_SCALE, v[3][q] * W8_SCALE); o.y = pk_fp8x4(v[4][q] * W8_SCALE, v[5][q] * W8_SCALE, v[6][q] * W8_SCALE, v[7][q] * W8_SCALE);
;             o.z = pk_fp8x4(v[8][q] * W8_SCALE, v[9][q] * W8_SCALE, v[10][q] * W8_SCALE, v[11][q] * W8_SCALE); o.w = pk_fp8x4(v[12][q] * W8_SCALE, v[13][q] * W8_SCALE, v[14][q] * W8_SCALE, v[15][q] * W8_SCALE);
;             *(LAS u32x4*)(buf + (4 * X.lane + q) * CVT_STRIDE + 16 * X.wave) = o; }
;         if (j + 1 < count) { cn = conv8b_dec(X, first + (j + 1) * step);
.LBB0_477:
	s_waitcnt vmcnt(0)
	v_mul_f32_e32 v79, 0x42800000, v62
	v_mul_f32_e32 v80, 0x42800000, v30
	v_med3_f32 v79, v79, s14, v78
	v_med3_f32 v82, v80, s14, v78
	v_mov_b32_e32 v80, 0
	v_cvt_pk_fp8_f32 v80, v79, v82
	v_mul_f32_e32 v81, 0x42800000, v26
	v_mul_f32_e32 v79, 0x42800000, v58
	v_med3_f32 v81, v81, s14, v78
	v_med3_f32 v79, v79, s14, v78
	v_cvt_pk_fp8_f32 v80, v81, v79 op_sel:[0,0,1]
	v_mul_f32_e32 v79, 0x42800000, v22
	v_mul_f32_e32 v81, 0x42800000, v54
	v_med3_f32 v79, v79, s14, v78
	v_med3_f32 v83, v81, s14, v78
	v_mov_b32_e32 v81, 0
	v_cvt_pk_fp8_f32 v81, v79, v83
	v_mul_f32_e32 v82, 0x42800000, v18
	v_mul_f32_e32 v79, 0x42800000, v50
	v_med3_f32 v82, v82, s14, v78
	v_med3_f32 v79, v79, s14, v78
	v_cvt_pk_fp8_f32 v81, v82, v79 op_sel:[0,0,1]
	v_mul_f32_e32 v79, 0x42800000, v14
	v_mul_f32_e32 v82, 0x42800000, v46
	v_med3_f32 v79, v79, s14, v78
	v_med3_f32 v84, v82, s14, v78
	v_mov_b32_e32 v82, 0
	v_cvt_pk_fp8_f32 v82, v79, v84
	v_mul_f32_e32 v83, 0x42800000, v10
	v_mul_f32_e32 v79, 0x42800000, v42
	v_med3_f32 v83, v83, s14, v78
	v_med3_f32 v79, v79, s14, v78
	v_cvt_pk_fp8_f32 v82, v83, v79 op_sel:[0,0,1]
	v_mul_f32_e32 v79, 0x42800000, v6
	v_mul_f32_e32 v83, 0x42800000, v38
	v_med3_f32 v79, v79, s14, v78
	v_med3_f32 v85, v83, s14, v78
	v_mov_b32_e32 v83, 0
	v_cvt_pk_fp8_f32 v83, v79, v85
	v_mul_f32_e32 v84, 0x42800000, v2
	v_mul_f32_e32 v79, 0x42800000, v34
	s_bitcmp1_b32 s16, 0
	v_med3_f32 v84, v84, s14, v78
	v_med3_f32 v79, v79, s14, v78
	s_cselect_b32 s2, 0x9000, 0
	v_cvt_pk_fp8_f32 v83, v84, v79 op_sel:[0,0,1]
	s_add_i32 s17, s2, 0
	s_add_i32 s2, s12, s17
	v_add_u32_e32 v79, s2, v76
	ds_write_b128 v79, v[80:83]
	v_mul_f32_e32 v80, 0x42800000, v63
	v_mul_f32_e32 v81, 0x42800000, v31
	v_med3_f32 v83, v80, s14, v78
	v_med3_f32 v81, v81, s14, v78
	v_mov_b32_e32 v80, 0
	v_cvt_pk_fp8_f32 v80, v83, v81
	v_mul_f32_e32 v82, 0x42800000, v27
	v_mul_f32_e32 v81, 0x42800000, v59
	v_med3_f32 v82, v82, s14, v78
	v_med3_f32 v81, v81, s14, v78
	v_cvt_pk_fp8_f32 v80, v82, v81 op_sel:[0,0,1]
	v_mul_f32_e32 v81, 0x42800000, v23
	v_mul_f32_e32 v82, 0x42800000, v55
	v_med3_f32 v84, v81, s14, v78
	v_med3_f32 v82, v82, s14, v78
	v_mov_b32_e32 v81, 0
	v_cvt_pk_fp8_f32 v81, v84, v82
	v_mul_f32_e32 v83, 0x42800000, v19
	v_mul_f32_e32 v82, 0x42800000, v51
	v_med3_f32 v83, v83, s14, v78
	v_med3_f32 v82, v82, s14, v78
	v_cvt_pk_fp8_f32 v81, v83, v82 op_sel:[0,0,1]
	v_mul_f32_e32 v82, 0x42800000, v15
	v_mul_f32_e32 v83, 0x42800000, v47
	v_med3_f32 v85, v82, s14, v78
	v_med3_f32 v83, v83, s14, v78
	v_mov_b32_e32 v82, 0
	v_cvt_pk_fp8_f32 v82, v85, v83
	v_mul_f32_e32 v84, 0x42800000, v11
	v_mul_f32_e32 v83, 0x42800000, v43
	v_med3_f32 v84, v84, s14, v78
	v_med3_f32 v83, v83, s14, v78
	v_cvt_pk_fp8_f32 v82, v84, v83 op_sel:[0,0,1]
	v_mul_f32_e32 v83, 0x42800000, v7
	v_mul_f32_e32 v84, 0x42800000, v39
	v_med3_f32 v86, v83, s14, v78
	v_med3_f32 v84, v84, s14, v78
	v_mov_b32_e32 v83, 0
	v_cvt_pk_fp8_f32 v83, v86, v84
	v_mul_f32_e32 v85, 0x42800000, v3
	v_mul_f32_e32 v84, 0x42800000, v35
	v_med3_f32 v85, v85, s14, v78
	v_med3_f32 v84, v84, s14, v78
	v_cvt_pk_fp8_f32 v83, v85, v84 op_sel:[0,0,1]
	v_mul_f32_e32 v84, 0x42800000, v64
	v_mul_f32_e32 v85, 0x42800000, v32
	v_med3_f32 v87, v84, s14, v78
	v_med3_f32 v85, v85, s14, v78
	v_mov_b32_e32 v84, 0
	v_cvt_pk_fp8_f32 v84, v87, v85
	v_mul_f32_e32 v86, 0x42800000, v28
	v_mul_f32_e32 v85, 0x42800000, v60
	v_med3_f32 v86, v86, s14, v78
	v_med3_f32 v85, v85, s14, v78
	v_cvt_pk_fp8_f32 v84, v86, v85 op_sel:[0,0,1]
	v_mul_f32_e32 v85, 0x42800000, v24
	v_mul_f32_e32 v86, 0x42800000, v56
	v_med3_f32 v88, v85, s14, v78
	v_med3_f32 v86, v86, s14, v78
	v_mov_b32_e32 v85, 0
	v_cvt_pk_fp8_f32 v85, v88, v86
	v_mul_f32_e32 v87, 0x42800000, v20
	v_mul_f32_e32 v86, 0x42800000, v52
	v_med3_f32 v87, v87, s14, v78
	v_med3_f32 v86, v86, s14, v78
	v_cvt_pk_fp8_f32 v85, v87, v86 op_sel:[0,0,1]
	v_mul_f32_e32 v86, 0x42800000, v16
	v_mul_f32_e32 v87, 0x42800000, v48
	v_med3_f32 v89, v86, s14, v78
	v_med3_f32 v87, v87, s14, v78
	v_mov_b32_e32 v86, 0
	v_cvt_pk_fp8_f32 v86, v89, v87
	v_mul_f32_e32 v88, 0x42800000, v12
	v_mul_f32_e32 v87, 0x42800000, v44
	v_med3_f32 v88, v88, s14, v78
	v_med3_f32 v87, v87, s14, v78
	v_cvt_pk_fp8_f32 v86, v88, v87 op_sel:[0,0,1]
	v_mul_f32_e32 v87, 0x42800000, v8
	v_mul_f32_e32 v88, 0x42800000, v40
	v_med3_f32 v90, v87, s14, v78
	v_med3_f32 v88, v88, s14, v78
	v_mov_b32_e32 v87, 0
	v_cvt_pk_fp8_f32 v87, v90, v88
	v_mul_f32_e32 v89, 0x42800000, v4
	v_mul_f32_e32 v88, 0x42800000, v36
	v_med3_f32 v89, v89, s14, v78
	v_med3_f32 v88, v88, s14, v78
	v_cvt_pk_fp8_f32 v87, v89, v88 op_sel:[0,0,1]
	v_mul_f32_e32 v88, 0x42800000, v65
	v_mul_f32_e32 v89, 0x42800000, v33
	v_med3_f32 v91, v88, s14, v78
	v_med3_f32 v89, v89, s14, v78
	v_mov_b32_e32 v88, 0
	v_cvt_pk_fp8_f32 v88, v91, v89
	v_mul_f32_e32 v90, 0x42800000, v29
	v_mul_f32_e32 v89, 0x42800000, v61
	v_med3_f32 v90, v90, s14, v78
	v_med3_f32 v89, v89, s14, v78
	v_cvt_pk_fp8_f32 v88, v90, v89 op_sel:[0,0,1]
	v_mul_f32_e32 v89, 0x42800000, v25
	v_mul_f32_e32 v90, 0x42800000, v57
	v_med3_f32 v92, v89, s14, v78
	v_med3_f32 v90, v90, s14, v78
	v_mov_b32_e32 v89, 0
	v_cvt_pk_fp8_f32 v89, v92, v90
	v_mul_f32_e32 v91, 0x42800000, v21
	v_mul_f32_e32 v90, 0x42800000, v53
	v_med3_f32 v91, v91, s14, v78
	v_med3_f32 v90, v90, s14, v78
	v_cvt_pk_fp8_f32 v89, v91, v90 op_sel:[0,0,1]
	v_mul_f32_e32 v90, 0x42800000, v17
	v_mul_f32_e32 v91, 0x42800000, v49
	v_med3_f32 v93, v90, s14, v78
	v_med3_f32 v91, v91, s14, v78
	v_mov_b32_e32 v90, 0
	v_cvt_pk_fp8_f32 v90, v93, v91
	v_mul_f32_e32 v92, 0x42800000, v13
	v_mul_f32_e32 v91, 0x42800000, v45
	v_med3_f32 v92, v92, s14, v78
	v_med3_f32 v91, v91, s14, v78
	v_cvt_pk_fp8_f32 v90, v92, v91 op_sel:[0,0,1]
	v_mul_f32_e32 v91, 0x42800000, v9
	v_mul_f32_e32 v92, 0x42800000, v41
	v_med3_f32 v94, v91, s14, v78
	v_med3_f32 v92, v92, s14, v78
	v_mov_b32_e32 v91, 0
	v_cvt_pk_fp8_f32 v91, v94, v92
	v_mul_f32_e32 v93, 0x42800000, v5
	v_mul_f32_e32 v92, 0x42800000, v37
	v_med3_f32 v93, v93, s14, v78
	v_med3_f32 v92, v92, s14, v78
	v_cvt_pk_fp8_f32 v91, v93, v92 op_sel:[0,0,1]
	s_cmp_ge_u32 s16, 0
	ds_write_b128 v79, v[80:83] offset:144
	ds_write_b128 v79, v[84:87] offset:288
	ds_write_b128 v79, v[88:91] offset:432
	s_cbranch_scc1 .LBB0_476
; __device__ __forceinline__ Cvb conv8b_dec(const Ctx& X, int bit) { Cvb c; int kb, nb;
;     if (bit < I_GU8 / 8) { const int e = bit >> 8, r = bit & 255; kb = r >> 4; nb = r & 15; c.N = 2 * DFF; c.W = XP_w_gu(X) + (size_t)e * D * (2 * DFF); c.WT = XP_WguT(X) + (size_t)e * 16 * PAN_GU + (size_t)kb * PAN_GU; }
;     else { const int b2 = bit - I_GU8 / 8, e = b2 >> 7, r = b2 & 127; kb = r >> 3; nb = r & 7; c.N = D; c.W = XP_w_d(X) + (size_t)e * DFF * D; c.WT = XP_WdT(X) + (size_t)e * 16 * PAN_D + (size_t)kb * PAN_D; }
;     c.W += (size_t)(kb * 128 + 16 * X.wave) * c.N + nb * 256 + 4 * X.lane;
;     c.WT += (size_t)(nb * 256 + 32 * X.wave + (X.lane >> 3)) * 128 + 16 * (X.lane & 7);
; __device__ __forceinline__ void conv8b_run(const Ctx& X, int first, int step, int count) {
;     ...
;         if (j + 1 < count) { cn = conv8b_dec(X, first + (j + 1) * step);
; #pragma unroll
;             for (int i = 0; i < 16; ++i) v[i] = __builtin_nontemporal_load((const f32x4*)(cn.W + (size_t)i * cn.N)); }
	s_add_i32 s2, s13, 0xffffe000
	s_load_dwordx2 s[6:7], s[0:1], 0x80
	s_bfe_u32 s18, s13, 0x40003
	s_lshr_b32 s2, s2, 7
	s_lshl_b32 s19, s18, 18
	s_lshl_b64 s[8:9], s[2:3], 22
	s_add_u32 s20, s10, s8
	s_addc_u32 s21, s11, s9
	s_lshl_b64 s[8:9], s[2:3], 24
	s_waitcnt lgkmcnt(0)
	s_add_u32 s22, s6, s8
	s_addc_u32 s23, s7, s9
	s_add_u32 s6, s20, s19
	s_addc_u32 s7, s21, 0
	s_lshl_b32 s2, s18, 7
	s_add_i32 s2, s2, s12
	s_lshl_b64 s[8:9], s[2:3], 13
	s_add_u32 s2, s22, s8
	s_addc_u32 s9, s23, s9
	s_add_u32 s8, s2, s15
	s_addc_u32 s9, s9, 0
	v_lshl_add_u64 v[34:35], s[8:9], 0, v[66:67]
	v_add_co_u32_e32 v2, vcc, 0x2000, v34
	s_nop 1
	v_addc_co_u32_e32 v3, vcc, 0, v35, vcc
	v_add_co_u32_e32 v4, vcc, 0x4000, v34
	s_nop 1
	v_addc_co_u32_e32 v5, vcc, 0, v35, vcc
	global_load_dwordx4 v[30:33], v[2:3], off nt
	global_load_dwordx4 v[26:29], v[4:5], off nt
	v_add_co_u32_e32 v2, vcc, 0x6000, v34
	s_nop 1
	v_addc_co_u32_e32 v3, vcc, 0, v35, vcc
	v_add_co_u32_e32 v4, vcc, 0x8000, v34
	s_nop 1
	v_addc_co_u32_e32 v5, vcc, 0, v35, vcc
	global_load_dwordx4 v[58:61], v[2:3], off nt
	global_load_dwordx4 v[22:25], v[4:5], off nt
	v_add_co_u32_e32 v2, vcc, 0xa000, v34
	s_nop 1
	v_addc_co_u32_e32 v3, vcc, 0, v35, vcc
	v_add_co_u32_e32 v4, vcc, 0xc000, v34
	s_nop 1
	v_addc_co_u32_e32 v5, vcc, 0, v35, vcc
	global_load_dwordx4 v[54:57], v[2:3], off nt
	global_load_dwordx4 v[18:21], v[4:5], off nt
	v_add_co_u32_e32 v2, vcc, 0xe000, v34
	s_nop 1
	v_addc_co_u32_e32 v3, vcc, 0, v35, vcc
	v_add_co_u32_e32 v4, vcc, 0x10000, v34
	s_nop 1
	v_addc_co_u32_e32 v5, vcc, 0, v35, vcc
	global_load_dwordx4 v[50:53], v[2:3], off nt
	global_load_dwordx4 v[14:17], v[4:5], off nt
	v_add_co_u32_e32 v2, vcc, 0x12000, v34
	s_nop 1
	v_addc_co_u32_e32 v3, vcc, 0, v35, vcc
	v_add_co_u32_e32 v4, vcc, 0x14000, v34
	s_nop 1
	v_addc_co_u32_e32 v5, vcc, 0, v35, vcc
	global_load_dwordx4 v[46:49], v[2:3], off nt
	global_load_dwordx4 v[10:13], v[4:5], off nt
	v_add_co_u32_e32 v2, vcc, 0x16000, v34
	s_nop 1
	v_addc_co_u32_e32 v3, vcc, 0, v35, vcc
	v_add_co_u32_e32 v4, vcc, 0x18000, v34
	s_nop 1
	v_addc_co_u32_e32 v5, vcc, 0, v35, vcc
	v_add_co_u32_e32 v36, vcc, 0x1a000, v34
	global_load_dwordx4 v[42:45], v[2:3], off nt
	global_load_dwordx4 v[6:9], v[4:5], off nt
	v_addc_co_u32_e32 v37, vcc, 0, v35, vcc
	v_add_co_u32_e32 v62, vcc, 0x1c000, v34
	s_nop 1
	v_addc_co_u32_e32 v63, vcc, 0, v35, vcc
	v_add_co_u32_e32 v74, vcc, 0x1e000, v34
	global_load_dwordx4 v[38:41], v[36:37], off nt
	global_load_dwordx4 v[2:5], v[62:63], off nt
	v_addc_co_u32_e32 v75, vcc, 0, v35, vcc
	global_load_dwordx4 v[62:65], v66, s[8:9] nt
	global_load_dwordx4 v[34:37], v[74:75], off nt
	v_lshl_add_u64 v[74:75], s[6:7], 0, v[70:71]
	v_lshl_add_u64 v[74:75], v[74:75], 0, v[68:69]
	s_branch .LBB0_476
